# DSA attn FIXM loop: separate fast loop with mask-word prefetch one tile ahead, K/V fragment ring reads, fin VALU between score MFMAs, exps+DMA in PV gaps
# speedup vs baseline: 1.0135x; 1.0135x over previous
.LBB0_1830:
	s_add_i32 s20, s65, -1
	s_cmp_lt_i32 s20, s22
	s_cbranch_scc1 .Lfs_entry
	s_cmp_le_i32 s20, s22
	s_cselect_b64 s[90:91], -1, 0
	s_cmp_gt_i32 s20, s22
	s_cbranch_scc1 .LBB0_1832
	global_load_dword v98, v[190:191], off
	v_add_co_u32_e32 v96, vcc, 0xffff0000, v190
	s_lshl_b32 s5, s89, 14
	s_nop 0
	v_addc_co_u32_e32 v97, vcc, -1, v191, vcc
	global_load_dword v96, v[96:97], off
	s_add_i32 s21, s5, 0
	v_add_u32_e32 v97, s21, v217
	ds_read_b128 v[222:225], v97 offset:49152
	ds_read_b128 v[112:115], v97 offset:57344
	v_add_u32_e32 v178, s21, v216
	s_waitcnt vmcnt(0)
	v_lshrrev_b32_e32 v97, v210, v98
	v_not_b32_e32 v97, v97
	v_bfe_i32 v98, v97, 0, 1
	v_bfe_i32 v99, v97, 1, 1
	v_bfe_i32 v100, v97, 2, 1
	v_bfe_i32 v101, v97, 3, 1
	v_bfe_i32 v102, v97, 8, 1
	v_bfe_i32 v103, v97, 9, 1
	v_bfe_i32 v104, v97, 10, 1
	v_bfe_i32 v105, v97, 11, 1
	v_bfe_i32 v106, v97, 16, 1
	v_bfe_i32 v107, v97, 17, 1
	v_bfe_i32 v108, v97, 18, 1
	v_bfe_i32 v109, v97, 19, 1
	v_bfe_i32 v110, v97, 24, 1
	v_bfe_i32 v111, v97, 25, 1
	v_bfe_i32 v116, v97, 26, 1
	v_lshrrev_b32_e32 v118, v210, v96
	v_bfe_i32 v117, v97, 27, 1
	v_and_b32 v96, s71, v98
	v_and_b32 v97, s71, v99
	v_and_b32 v98, s71, v100
	v_and_b32 v99, s71, v101
	v_and_b32 v100, s71, v102
	v_and_b32 v101, s71, v103
	v_and_b32 v102, s71, v104
	v_and_b32 v103, s71, v105
	v_and_b32 v104, s71, v106
	v_and_b32 v105, s71, v107
	v_and_b32 v106, s71, v108
	v_and_b32 v107, s71, v109
	v_and_b32 v108, s71, v110
	v_and_b32 v109, s71, v111
	v_and_b32 v110, s71, v116
	v_and_b32 v111, s71, v117
	v_not_b32_e32 v116, v118
	s_waitcnt lgkmcnt(0)
	v_mfma_f32_32x32x16_bf16 v[96:111], v[112:115], v[156:159], v[96:111]
	v_bfe_i32 v112, v116, 0, 1
	v_bfe_i32 v113, v116, 1, 1
	v_bfe_i32 v114, v116, 2, 1
	v_bfe_i32 v115, v116, 3, 1
	v_bfe_i32 v117, v116, 8, 1
	v_bfe_i32 v118, v116, 9, 1
	v_bfe_i32 v119, v116, 10, 1
	v_bfe_i32 v120, v116, 11, 1
	v_bfe_i32 v121, v116, 16, 1
	v_bfe_i32 v122, v116, 17, 1
	v_bfe_i32 v123, v116, 18, 1
	v_bfe_i32 v124, v116, 19, 1
	v_bfe_i32 v125, v116, 24, 1
	v_bfe_i32 v126, v116, 25, 1
	v_bfe_i32 v127, v116, 26, 1
	v_bfe_i32 v179, v116, 27, 1
	v_and_b32 v112, s71, v112
	v_and_b32 v113, s71, v113
	v_and_b32 v114, s71, v114
	v_and_b32 v115, s71, v115
	v_and_b32 v116, s71, v117
	v_and_b32 v117, s71, v118
	v_and_b32 v118, s71, v119
	v_and_b32 v119, s71, v120
	v_and_b32 v120, s71, v121
	v_and_b32 v121, s71, v122
	v_and_b32 v122, s71, v123
	v_and_b32 v123, s71, v124
	v_and_b32 v124, s71, v125
	v_and_b32 v125, s71, v126
	v_and_b32 v126, s71, v127
	v_and_b32 v127, s71, v179
	s_nop 0
	v_mfma_f32_32x32x16_bf16 v[112:127], v[222:225], v[156:159], v[112:127]
	ds_read_b128 v[222:225], v178 offset:57344
	s_waitcnt lgkmcnt(0)
	v_mfma_f32_32x32x16_bf16 v[96:111], v[222:225], v[152:155], v[96:111]
	ds_read_b128 v[222:225], v178 offset:49152
	v_add_u32_e32 v178, s21, v215
	s_waitcnt lgkmcnt(0)
	v_mfma_f32_32x32x16_bf16 v[112:127], v[222:225], v[152:155], v[112:127]
	ds_read_b128 v[222:225], v178 offset:57344
	s_waitcnt lgkmcnt(0)
	v_mfma_f32_32x32x16_bf16 v[96:111], v[222:225], v[148:151], v[96:111]
	ds_read_b128 v[222:225], v178 offset:49152
	v_add_u32_e32 v178, s21, v214
	s_waitcnt lgkmcnt(0)
	v_mfma_f32_32x32x16_bf16 v[112:127], v[222:225], v[148:151], v[112:127]
	ds_read_b128 v[222:225], v178 offset:57344
	s_waitcnt lgkmcnt(0)
	v_mfma_f32_32x32x16_bf16 v[96:111], v[222:225], v[144:147], v[96:111]
	ds_read_b128 v[222:225], v178 offset:49152
	v_add_u32_e32 v178, s21, v220
	s_waitcnt lgkmcnt(0)
	v_mfma_f32_32x32x16_bf16 v[112:127], v[222:225], v[144:147], v[112:127]
	ds_read_b128 v[222:225], v178 offset:57344
	s_waitcnt lgkmcnt(0)
	v_mfma_f32_32x32x16_bf16 v[96:111], v[222:225], v[140:143], v[96:111]
	ds_read_b128 v[222:225], v178 offset:49152
	v_add_u32_e32 v178, s21, v218
	s_waitcnt lgkmcnt(0)
	v_mfma_f32_32x32x16_bf16 v[112:127], v[222:225], v[140:143], v[112:127]
	ds_read_b128 v[222:225], v178 offset:57344
	s_waitcnt lgkmcnt(0)
	v_mfma_f32_32x32x16_bf16 v[96:111], v[222:225], v[136:139], v[96:111]
	ds_read_b128 v[222:225], v178 offset:49152
	v_add_u32_e32 v178, s21, v219
	s_waitcnt lgkmcnt(0)
	v_mfma_f32_32x32x16_bf16 v[112:127], v[222:225], v[136:139], v[112:127]
	ds_read_b128 v[222:225], v178 offset:57344
	s_waitcnt lgkmcnt(0)
	v_mfma_f32_32x32x16_bf16 v[96:111], v[222:225], v[132:135], v[96:111]
	ds_read_b128 v[222:225], v178 offset:49152
	v_add_u32_e32 v178, s21, v221
	s_waitcnt lgkmcnt(0)
	v_mfma_f32_32x32x16_bf16 v[112:127], v[222:225], v[132:135], v[112:127]
	ds_read_b128 v[222:225], v178 offset:49152
	s_waitcnt lgkmcnt(0)
	v_mfma_f32_32x32x16_bf16 v[112:127], v[222:225], v[128:131], v[112:127]
	ds_read_b128 v[222:225], v178 offset:57344
	s_waitcnt lgkmcnt(0)
	v_mfma_f32_32x32x16_bf16 v[96:111], v[222:225], v[128:131], v[96:111]

.Lfs_entry:
	global_load_dword v180, v[190:191], off
	v_add_co_u32_e32 v250, vcc, 0xffff0000, v190
	s_nop 1
	v_addc_co_u32_e32 v251, vcc, -1, v191, vcc
	global_load_dword v179, v[250:251], off
	s_waitcnt vmcnt(0)
.Lfs_loop:
	s_lshl_b32 s21, s15, 14
	v_add_u32_e32 v181, s21, v213
	s_lshl_b32 s5, s89, 14
	v_add_u32_e32 v178, s5, v217
	ds_read_b128 v[238:241], v178 offset:49152
	ds_read_b128 v[242:245], v178 offset:57344
	v_add_u32_e32 v178, s5, v216
	ds_read_b128 v[246:249], v178 offset:49152
	ds_read_b128 v[222:225], v178 offset:57344
	v_add_u32_e32 v178, s5, v215
	ds_read_b128 v[226:229], v178 offset:49152
	ds_read_b128 v[230:233], v178 offset:57344
	v_lshrrev_b32_e32 v196, v210, v179
	v_not_b32_e32 v196, v196
	v_bfe_i32 v112, v196, 0, 1
	v_bfe_i32 v113, v196, 1, 1
	v_and_b32_e32 v112, s71, v112
	v_and_b32_e32 v113, s71, v113
	v_bfe_i32 v114, v196, 2, 1
	v_bfe_i32 v115, v196, 3, 1
	v_and_b32_e32 v114, s71, v114
	v_and_b32_e32 v115, s71, v115
	v_bfe_i32 v116, v196, 8, 1
	v_bfe_i32 v117, v196, 9, 1
	v_and_b32_e32 v116, s71, v116
	v_and_b32_e32 v117, s71, v117
	v_bfe_i32 v118, v196, 10, 1
	v_bfe_i32 v119, v196, 11, 1
	v_and_b32_e32 v118, s71, v118
	v_and_b32_e32 v119, s71, v119
	v_bfe_i32 v120, v196, 16, 1
	v_bfe_i32 v121, v196, 17, 1
	v_and_b32_e32 v120, s71, v120
	v_and_b32_e32 v121, s71, v121
	v_bfe_i32 v122, v196, 18, 1
	v_bfe_i32 v123, v196, 19, 1
	v_and_b32_e32 v122, s71, v122
	v_and_b32_e32 v123, s71, v123
	v_bfe_i32 v124, v196, 24, 1
	v_bfe_i32 v125, v196, 25, 1
	v_and_b32_e32 v124, s71, v124
	v_and_b32_e32 v125, s71, v125
	v_bfe_i32 v126, v196, 26, 1
	v_bfe_i32 v127, v196, 27, 1
	v_and_b32_e32 v126, s71, v126
	v_and_b32_e32 v127, s71, v127
	v_lshrrev_b32_e32 v196, v210, v180
	v_not_b32_e32 v196, v196
	v_bfe_i32 v96, v196, 0, 1
	v_bfe_i32 v97, v196, 1, 1
	v_and_b32_e32 v96, s71, v96
	v_and_b32_e32 v97, s71, v97
	v_bfe_i32 v98, v196, 2, 1
	v_bfe_i32 v99, v196, 3, 1
	v_and_b32_e32 v98, s71, v98
	v_and_b32_e32 v99, s71, v99
	v_bfe_i32 v100, v196, 8, 1
	v_bfe_i32 v101, v196, 9, 1
	v_and_b32_e32 v100, s71, v100
	v_and_b32_e32 v101, s71, v101
	v_bfe_i32 v102, v196, 10, 1
	v_bfe_i32 v103, v196, 11, 1
	v_and_b32_e32 v102, s71, v102
	v_and_b32_e32 v103, s71, v103
	v_bfe_i32 v104, v196, 16, 1
	v_bfe_i32 v105, v196, 17, 1
	v_and_b32_e32 v104, s71, v104
	v_and_b32_e32 v105, s71, v105
	v_bfe_i32 v106, v196, 18, 1
	v_bfe_i32 v107, v196, 19, 1
	v_and_b32_e32 v106, s71, v106
	v_and_b32_e32 v107, s71, v107
	v_bfe_i32 v108, v196, 24, 1
	v_bfe_i32 v109, v196, 25, 1
	v_and_b32_e32 v108, s71, v108
	v_and_b32_e32 v109, s71, v109
	v_bfe_i32 v110, v196, 26, 1
	v_bfe_i32 v111, v196, 27, 1
	v_and_b32_e32 v110, s71, v110
	v_and_b32_e32 v111, s71, v111
	s_add_i32 s72, s88, -1
	s_lshl_b64 s[56:57], s[72:73], 16
	v_lshl_add_u64 v[250:251], v[184:185], 0, s[56:57]
	s_add_i32 s72, s88, 0
	s_lshl_b64 s[56:57], s[72:73], 16
	global_load_dword v179, v[250:251], off
	v_lshl_add_u64 v[250:251], v[184:185], 0, s[56:57]
	s_nop 0
	global_load_dword v180, v[250:251], off
	s_waitcnt lgkmcnt(5)
	v_mfma_f32_32x32x16_bf16 v[112:127], v[238:241], v[156:159], v[112:127]
	v_add_u32_e32 v178, s5, v214
	ds_read_b128 v[234:237], v178 offset:49152
	v_add_f32_e32 v160, 0, v80
	v_add_f32_e32 v160, v81, v160
	v_add_f32_e32 v160, v82, v160
	v_add_f32_e32 v160, v83, v160
	s_waitcnt lgkmcnt(5)
	v_mfma_f32_32x32x16_bf16 v[96:111], v[242:245], v[156:159], v[96:111]
	ds_read_b128 v[238:241], v178 offset:57344
	v_add_f32_e32 v160, v84, v160
	v_add_f32_e32 v160, v85, v160
	v_add_f32_e32 v160, v86, v160
	v_add_f32_e32 v160, v87, v160
	s_waitcnt lgkmcnt(5)
	v_mfma_f32_32x32x16_bf16 v[112:127], v[246:249], v[152:155], v[112:127]
	v_add_u32_e32 v178, s5, v220
	ds_read_b128 v[242:245], v178 offset:49152
	v_add_f32_e32 v160, v88, v160
	v_add_f32_e32 v160, v89, v160
	v_add_f32_e32 v160, v90, v160
	v_add_f32_e32 v160, v91, v160
	s_waitcnt lgkmcnt(5)
	v_mfma_f32_32x32x16_bf16 v[96:111], v[222:225], v[152:155], v[96:111]
	ds_read_b128 v[246:249], v178 offset:57344
	v_exp_f32_e32 v64, v64
	v_add_f32_e32 v160, v92, v160
	v_exp_f32_e32 v65, v65
	v_add_f32_e32 v160, v93, v160
	s_waitcnt lgkmcnt(5)
	v_mfma_f32_32x32x16_bf16 v[112:127], v[226:229], v[148:151], v[112:127]
	v_add_u32_e32 v178, s5, v218
	ds_read_b128 v[222:225], v178 offset:49152
	v_exp_f32_e32 v66, v66
	v_add_f32_e32 v160, v94, v160
	v_exp_f32_e32 v67, v67
	v_add_f32_e32 v160, v95, v160
	s_waitcnt lgkmcnt(5)
	v_mfma_f32_32x32x16_bf16 v[96:111], v[230:233], v[148:151], v[96:111]
	ds_read_b128 v[226:229], v178 offset:57344
	v_exp_f32_e32 v68, v68
	v_add_f32_e32 v160, v64, v160
	v_exp_f32_e32 v69, v69
	v_add_f32_e32 v160, v65, v160
	s_waitcnt lgkmcnt(5)
	v_mfma_f32_32x32x16_bf16 v[112:127], v[234:237], v[144:147], v[112:127]
	v_add_u32_e32 v178, s5, v219
	ds_read_b128 v[230:233], v178 offset:49152
	v_exp_f32_e32 v70, v70
	v_add_f32_e32 v160, v66, v160
	v_exp_f32_e32 v71, v71
	v_add_f32_e32 v160, v67, v160
	s_waitcnt lgkmcnt(5)
	v_mfma_f32_32x32x16_bf16 v[96:111], v[238:241], v[144:147], v[96:111]
	ds_read_b128 v[234:237], v178 offset:57344
	v_exp_f32_e32 v72, v72
	v_add_f32_e32 v160, v68, v160
	v_exp_f32_e32 v73, v73
	v_add_f32_e32 v160, v69, v160
	s_waitcnt lgkmcnt(5)
	v_mfma_f32_32x32x16_bf16 v[112:127], v[242:245], v[140:143], v[112:127]
	v_add_u32_e32 v178, s5, v221
	ds_read_b128 v[238:241], v178 offset:49152
	v_exp_f32_e32 v74, v74
	v_add_f32_e32 v160, v70, v160
	v_exp_f32_e32 v75, v75
	v_add_f32_e32 v160, v71, v160
	s_waitcnt lgkmcnt(5)
	v_mfma_f32_32x32x16_bf16 v[96:111], v[246:249], v[140:143], v[96:111]
	ds_read_b128 v[242:245], v178 offset:57344
	v_exp_f32_e32 v76, v76
	v_add_f32_e32 v160, v72, v160
	v_exp_f32_e32 v77, v77
	v_add_f32_e32 v160, v73, v160
	s_waitcnt lgkmcnt(5)
	v_mfma_f32_32x32x16_bf16 v[112:127], v[222:225], v[136:139], v[112:127]
	v_exp_f32_e32 v78, v78
	v_add_f32_e32 v160, v74, v160
	v_exp_f32_e32 v79, v79
	v_add_f32_e32 v160, v75, v160
	s_waitcnt lgkmcnt(4)
	v_mfma_f32_32x32x16_bf16 v[96:111], v[226:229], v[136:139], v[96:111]
	v_add_f32_e32 v160, v76, v160
	v_add_f32_e32 v160, v77, v160
	v_add_f32_e32 v160, v78, v160
	v_add_f32_e32 v160, v79, v160
	s_waitcnt lgkmcnt(3)
	v_mfma_f32_32x32x16_bf16 v[112:127], v[230:233], v[132:135], v[112:127]
	v_mov_b32_e32 v161, v160
	s_nop 1
	v_permlane32_swap_b32_e32 v160, v161
	v_add_f32_e32 v160, v160, v161
	s_waitcnt lgkmcnt(2)
	v_mfma_f32_32x32x16_bf16 v[96:111], v[234:237], v[132:135], v[96:111]
	ds_read_b64_tr_b16 v[222:223], v181 offset:0
	ds_read_b64_tr_b16 v[224:225], v181 offset:2048
	ds_read_b64_tr_b16 v[226:227], v181 offset:4096
	ds_read_b64_tr_b16 v[228:229], v181 offset:6144
	ds_read_b64_tr_b16 v[230:231], v181 offset:8192
	ds_read_b64_tr_b16 v[232:233], v181 offset:10240
	ds_read_b64_tr_b16 v[234:235], v181 offset:12288
	ds_read_b64_tr_b16 v[236:237], v181 offset:14336
	v_add_f32_e32 v212, v212, v160
	v_cvt_pk_bf16_f32 v160, v80, v81
	v_cvt_pk_bf16_f32 v161, v82, v83
	v_cvt_pk_bf16_f32 v162, v84, v85
	s_waitcnt lgkmcnt(9)
	v_mfma_f32_32x32x16_bf16 v[112:127], v[238:241], v[128:131], v[112:127]
	v_cvt_pk_bf16_f32 v163, v86, v87
	v_cvt_pk_bf16_f32 v164, v88, v89
	v_cvt_pk_bf16_f32 v165, v90, v91
	v_cvt_pk_bf16_f32 v166, v92, v93
	s_waitcnt lgkmcnt(8)
	v_mfma_f32_32x32x16_bf16 v[96:111], v[242:245], v[128:131], v[96:111]
	v_cvt_pk_bf16_f32 v167, v94, v95
	v_cvt_pk_bf16_f32 v168, v64, v65
	v_cvt_pk_bf16_f32 v169, v66, v67
	v_cvt_pk_bf16_f32 v170, v68, v69
	ds_read_b64_tr_b16 v[246:247], v181 offset:512
	ds_read_b64_tr_b16 v[248:249], v181 offset:2560
	v_cvt_pk_bf16_f32 v171, v70, v71
	v_cvt_pk_bf16_f32 v172, v72, v73
	v_cvt_pk_bf16_f32 v173, v74, v75
	v_cvt_pk_bf16_f32 v174, v76, v77
	v_cvt_pk_bf16_f32 v175, v78, v79
	s_nop 0
	v_permlane32_swap_b32_e32 v160, v162
	v_permlane32_swap_b32_e32 v161, v163
	v_permlane32_swap_b32_e32 v164, v166
	v_permlane32_swap_b32_e32 v165, v167
	v_permlane32_swap_b32_e32 v168, v170
	v_permlane32_swap_b32_e32 v169, v171
	v_permlane32_swap_b32_e32 v172, v174
	v_permlane32_swap_b32_e32 v173, v175
	s_waitcnt lgkmcnt(8)
	v_mfma_f32_32x32x16_bf16 v[48:63], v[160:163], v[222:225], v[48:63]
	ds_read_b64_tr_b16 v[238:239], v181 offset:4608
	ds_read_b64_tr_b16 v[240:241], v181 offset:6656
	v_exp_f32_e32 v112, v112
	s_waitcnt lgkmcnt(8)
	v_mfma_f32_32x32x16_bf16 v[48:63], v[164:167], v[226:229], v[48:63]
	ds_read_b64_tr_b16 v[222:223], v181 offset:8704
	ds_read_b64_tr_b16 v[224:225], v181 offset:10752
	v_exp_f32_e32 v113, v113
	s_add_i32 s5, s65, 1
	s_min_i32 s5, s5, s92
	s_lshl_b32 s72, s5, 16
	s_lshl_b32 s5, s89, 14
	s_addk_i32 s5, 0xc000
	s_cmp_gt_i32 s89, 0
	s_cselect_b32 s5, s5, 0x8000
	s_add_i32 s5, s64, s5
	s_add_i32 m0, s5, 0xc000
	s_add_u32 s56, s34, s72
	s_addc_u32 s57, s35, 0
	v_lshl_add_u64 v[250:251], v[186:187], 0, s[72:73]
	s_nop 0
	global_load_lds_dwordx4 v[250:251], off
	s_waitcnt lgkmcnt(8)
	v_mfma_f32_32x32x16_bf16 v[48:63], v[168:171], v[230:233], v[48:63]
	ds_read_b64_tr_b16 v[226:227], v181 offset:12800
	ds_read_b64_tr_b16 v[228:229], v181 offset:14848
	v_exp_f32_e32 v114, v114
	v_lshl_add_u64 v[250:251], v[176:177], 1, s[56:57]
	s_add_i32 m0, s5, 0xe000
	v_lshl_add_u64 v[250:251], v[250:251], 0, s[80:81]
	s_nop 0
	global_load_lds_dwordx4 v[250:251], off
	s_waitcnt lgkmcnt(8)
	v_mfma_f32_32x32x16_bf16 v[48:63], v[172:175], v[234:237], v[48:63]
	ds_read_b64_tr_b16 v[230:231], v181 offset:1024
	ds_read_b64_tr_b16 v[232:233], v181 offset:3072
	v_exp_f32_e32 v115, v115
	s_mov_b32 s87, s73
	s_lshl_b64 s[56:57], s[86:87], 10
	s_lshl_b32 s21, s15, 14
	s_add_i32 s5, s21, 0xffffc000
	s_cmp_gt_i32 s15, 0
	s_cselect_b32 s5, s5, 0x8000
	s_add_i32 s5, s64, s5
	v_lshl_add_u64 v[250:251], v[188:189], 0, s[56:57]
	s_mov_b32 m0, s5
	s_nop 0
	global_load_lds_dwordx4 v[250:251], off
	s_waitcnt lgkmcnt(8)
	v_mfma_f32_32x32x16_bf16 v[32:47], v[160:163], v[246:249], v[32:47]
	ds_read_b64_tr_b16 v[234:235], v181 offset:5120
	ds_read_b64_tr_b16 v[236:237], v181 offset:7168
	v_exp_f32_e32 v116, v116
	s_add_i32 s72, s86, 32
	s_lshl_b64 s[56:57], s[72:73], 10
	v_lshl_add_u64 v[250:251], v[188:189], 0, s[56:57]
	s_add_i32 m0, s5, 0x2000
	s_nop 0
	global_load_lds_dwordx4 v[250:251], off
	s_waitcnt lgkmcnt(8)
	v_mfma_f32_32x32x16_bf16 v[32:47], v[164:167], v[238:241], v[32:47]
	ds_read_b64_tr_b16 v[246:247], v181 offset:9216
	ds_read_b64_tr_b16 v[248:249], v181 offset:11264
	v_exp_f32_e32 v117, v117
	s_waitcnt lgkmcnt(8)
	v_mfma_f32_32x32x16_bf16 v[32:47], v[168:171], v[222:225], v[32:47]
	ds_read_b64_tr_b16 v[238:239], v181 offset:13312
	ds_read_b64_tr_b16 v[240:241], v181 offset:15360
	v_exp_f32_e32 v118, v118
	s_waitcnt lgkmcnt(8)
	v_mfma_f32_32x32x16_bf16 v[32:47], v[172:175], v[226:229], v[32:47]
	ds_read_b64_tr_b16 v[222:223], v181 offset:1536
	ds_read_b64_tr_b16 v[224:225], v181 offset:3584
	v_exp_f32_e32 v119, v119
	s_waitcnt lgkmcnt(8)
	v_mfma_f32_32x32x16_bf16 v[16:31], v[160:163], v[230:233], v[16:31]
	ds_read_b64_tr_b16 v[226:227], v181 offset:5632
	ds_read_b64_tr_b16 v[228:229], v181 offset:7680
	v_exp_f32_e32 v120, v120
	s_waitcnt lgkmcnt(8)
	v_mfma_f32_32x32x16_bf16 v[16:31], v[164:167], v[234:237], v[16:31]
	ds_read_b64_tr_b16 v[230:231], v181 offset:9728
	ds_read_b64_tr_b16 v[232:233], v181 offset:11776
	v_exp_f32_e32 v121, v121
	s_waitcnt lgkmcnt(8)
	v_mfma_f32_32x32x16_bf16 v[16:31], v[168:171], v[246:249], v[16:31]
	ds_read_b64_tr_b16 v[234:235], v181 offset:13824
	ds_read_b64_tr_b16 v[236:237], v181 offset:15872
	v_exp_f32_e32 v122, v122
	s_waitcnt lgkmcnt(8)
	v_mfma_f32_32x32x16_bf16 v[16:31], v[172:175], v[238:241], v[16:31]
	v_exp_f32_e32 v123, v123
	s_waitcnt lgkmcnt(6)
	v_mfma_f32_32x32x16_bf16 v[0:15], v[160:163], v[222:225], v[0:15]
	v_exp_f32_e32 v124, v124
	s_waitcnt lgkmcnt(4)
	v_mfma_f32_32x32x16_bf16 v[0:15], v[164:167], v[226:229], v[0:15]
	v_exp_f32_e32 v125, v125
	s_waitcnt lgkmcnt(2)
	v_mfma_f32_32x32x16_bf16 v[0:15], v[168:171], v[230:233], v[0:15]
	v_exp_f32_e32 v126, v126
	s_waitcnt lgkmcnt(0)
	v_mfma_f32_32x32x16_bf16 v[0:15], v[172:175], v[234:237], v[0:15]
	v_exp_f32_e32 v127, v127
	s_add_i32 s5, s89, 1
	s_waitcnt vmcnt(4) lgkmcnt(0)
	s_barrier
	s_cmp_lt_i32 s89, 2
	s_cselect_b32 s87, s5, 0
	s_add_i32 s5, s15, 1
	s_cmp_lt_i32 s15, 2
	s_cselect_b32 s15, s5, 0
	s_add_i32 s65, s65, 2
	s_lshl_b32 s20, s15, 14
	v_add_u32_e32 v181, s20, v213
	s_lshl_b32 s5, s87, 14
	v_add_u32_e32 v178, s5, v217
	ds_read_b128 v[238:241], v178 offset:49152
	ds_read_b128 v[242:245], v178 offset:57344
	v_add_u32_e32 v178, s5, v216
	ds_read_b128 v[246:249], v178 offset:49152
	ds_read_b128 v[222:225], v178 offset:57344
	v_add_u32_e32 v178, s5, v215
	ds_read_b128 v[226:229], v178 offset:49152
	ds_read_b128 v[230:233], v178 offset:57344
	v_lshrrev_b32_e32 v196, v210, v179
	v_not_b32_e32 v196, v196
	v_bfe_i32 v80, v196, 0, 1
	v_bfe_i32 v81, v196, 1, 1
	v_and_b32_e32 v80, s71, v80
	v_and_b32_e32 v81, s71, v81
	v_bfe_i32 v82, v196, 2, 1
	v_bfe_i32 v83, v196, 3, 1
	v_and_b32_e32 v82, s71, v82
	v_and_b32_e32 v83, s71, v83
	v_bfe_i32 v84, v196, 8, 1
	v_bfe_i32 v85, v196, 9, 1
	v_and_b32_e32 v84, s71, v84
	v_and_b32_e32 v85, s71, v85
	v_bfe_i32 v86, v196, 10, 1
	v_bfe_i32 v87, v196, 11, 1
	v_and_b32_e32 v86, s71, v86
	v_and_b32_e32 v87, s71, v87
	v_bfe_i32 v88, v196, 16, 1
	v_bfe_i32 v89, v196, 17, 1
	v_and_b32_e32 v88, s71, v88
	v_and_b32_e32 v89, s71, v89
	v_bfe_i32 v90, v196, 18, 1
	v_bfe_i32 v91, v196, 19, 1
	v_and_b32_e32 v90, s71, v90
	v_and_b32_e32 v91, s71, v91
	v_bfe_i32 v92, v196, 24, 1
	v_bfe_i32 v93, v196, 25, 1
	v_and_b32_e32 v92, s71, v92
	v_and_b32_e32 v93, s71, v93
	v_bfe_i32 v94, v196, 26, 1
	v_bfe_i32 v95, v196, 27, 1
	v_and_b32_e32 v94, s71, v94
	v_and_b32_e32 v95, s71, v95
	v_lshrrev_b32_e32 v196, v210, v180
	v_not_b32_e32 v196, v196
	v_bfe_i32 v64, v196, 0, 1
	v_bfe_i32 v65, v196, 1, 1
	v_and_b32_e32 v64, s71, v64
	v_and_b32_e32 v65, s71, v65
	v_bfe_i32 v66, v196, 2, 1
	v_bfe_i32 v67, v196, 3, 1
	v_and_b32_e32 v66, s71, v66
	v_and_b32_e32 v67, s71, v67
	v_bfe_i32 v68, v196, 8, 1
	v_bfe_i32 v69, v196, 9, 1
	v_and_b32_e32 v68, s71, v68
	v_and_b32_e32 v69, s71, v69
	v_bfe_i32 v70, v196, 10, 1
	v_bfe_i32 v71, v196, 11, 1
	v_and_b32_e32 v70, s71, v70
	v_and_b32_e32 v71, s71, v71
	v_bfe_i32 v72, v196, 16, 1
	v_bfe_i32 v73, v196, 17, 1
	v_and_b32_e32 v72, s71, v72
	v_and_b32_e32 v73, s71, v73
	v_bfe_i32 v74, v196, 18, 1
	v_bfe_i32 v75, v196, 19, 1
	v_and_b32_e32 v74, s71, v74
	v_and_b32_e32 v75, s71, v75
	v_bfe_i32 v76, v196, 24, 1
	v_bfe_i32 v77, v196, 25, 1
	v_and_b32_e32 v76, s71, v76
	v_and_b32_e32 v77, s71, v77
	v_bfe_i32 v78, v196, 26, 1
	v_bfe_i32 v79, v196, 27, 1
	v_and_b32_e32 v78, s71, v78
	v_and_b32_e32 v79, s71, v79
	s_add_i32 s72, s88, 1
	s_lshl_b64 s[56:57], s[72:73], 16
	v_lshl_add_u64 v[250:251], v[184:185], 0, s[56:57]
	s_add_i32 s72, s88, 2
	s_lshl_b64 s[56:57], s[72:73], 16
	global_load_dword v179, v[250:251], off
	v_lshl_add_u64 v[250:251], v[184:185], 0, s[56:57]
	s_nop 0
	global_load_dword v180, v[250:251], off
	s_waitcnt lgkmcnt(5)
	v_mfma_f32_32x32x16_bf16 v[80:95], v[238:241], v[156:159], v[80:95]
	v_add_u32_e32 v178, s5, v214
	ds_read_b128 v[234:237], v178 offset:49152
	v_add_f32_e32 v160, 0, v112
	v_add_f32_e32 v160, v113, v160
	v_add_f32_e32 v160, v114, v160
	v_add_f32_e32 v160, v115, v160
	s_waitcnt lgkmcnt(5)
	v_mfma_f32_32x32x16_bf16 v[64:79], v[242:245], v[156:159], v[64:79]
	ds_read_b128 v[238:241], v178 offset:57344
	v_add_f32_e32 v160, v116, v160
	v_add_f32_e32 v160, v117, v160
	v_add_f32_e32 v160, v118, v160
	v_add_f32_e32 v160, v119, v160
	s_waitcnt lgkmcnt(5)
	v_mfma_f32_32x32x16_bf16 v[80:95], v[246:249], v[152:155], v[80:95]
	v_add_u32_e32 v178, s5, v220
	ds_read_b128 v[242:245], v178 offset:49152
	v_add_f32_e32 v160, v120, v160
	v_add_f32_e32 v160, v121, v160
	v_add_f32_e32 v160, v122, v160
	v_add_f32_e32 v160, v123, v160
	s_waitcnt lgkmcnt(5)
	v_mfma_f32_32x32x16_bf16 v[64:79], v[222:225], v[152:155], v[64:79]
	ds_read_b128 v[246:249], v178 offset:57344
	v_exp_f32_e32 v96, v96
	v_add_f32_e32 v160, v124, v160
	v_exp_f32_e32 v97, v97
	v_add_f32_e32 v160, v125, v160
	s_waitcnt lgkmcnt(5)
	v_mfma_f32_32x32x16_bf16 v[80:95], v[226:229], v[148:151], v[80:95]
	v_add_u32_e32 v178, s5, v218
	ds_read_b128 v[222:225], v178 offset:49152
	v_exp_f32_e32 v98, v98
	v_add_f32_e32 v160, v126, v160
	v_exp_f32_e32 v99, v99
	v_add_f32_e32 v160, v127, v160
	s_waitcnt lgkmcnt(5)
	v_mfma_f32_32x32x16_bf16 v[64:79], v[230:233], v[148:151], v[64:79]
	ds_read_b128 v[226:229], v178 offset:57344
	v_exp_f32_e32 v100, v100
	v_add_f32_e32 v160, v96, v160
	v_exp_f32_e32 v101, v101
	v_add_f32_e32 v160, v97, v160
	s_waitcnt lgkmcnt(5)
	v_mfma_f32_32x32x16_bf16 v[80:95], v[234:237], v[144:147], v[80:95]
	v_add_u32_e32 v178, s5, v219
	ds_read_b128 v[230:233], v178 offset:49152
	v_exp_f32_e32 v102, v102
	v_add_f32_e32 v160, v98, v160
	v_exp_f32_e32 v103, v103
	v_add_f32_e32 v160, v99, v160
	s_waitcnt lgkmcnt(5)
	v_mfma_f32_32x32x16_bf16 v[64:79], v[238:241], v[144:147], v[64:79]
	ds_read_b128 v[234:237], v178 offset:57344
	v_exp_f32_e32 v104, v104
	v_add_f32_e32 v160, v100, v160
	v_exp_f32_e32 v105, v105
	v_add_f32_e32 v160, v101, v160
	s_waitcnt lgkmcnt(5)
	v_mfma_f32_32x32x16_bf16 v[80:95], v[242:245], v[140:143], v[80:95]
	v_add_u32_e32 v178, s5, v221
	ds_read_b128 v[238:241], v178 offset:49152
	v_exp_f32_e32 v106, v106
	v_add_f32_e32 v160, v102, v160
	v_exp_f32_e32 v107, v107
	v_add_f32_e32 v160, v103, v160
	s_waitcnt lgkmcnt(5)
	v_mfma_f32_32x32x16_bf16 v[64:79], v[246:249], v[140:143], v[64:79]
	ds_read_b128 v[242:245], v178 offset:57344
	v_exp_f32_e32 v108, v108
	v_add_f32_e32 v160, v104, v160
	v_exp_f32_e32 v109, v109
	v_add_f32_e32 v160, v105, v160
	s_waitcnt lgkmcnt(5)
	v_mfma_f32_32x32x16_bf16 v[80:95], v[222:225], v[136:139], v[80:95]
	v_exp_f32_e32 v110, v110
	v_add_f32_e32 v160, v106, v160
	v_exp_f32_e32 v111, v111
	v_add_f32_e32 v160, v107, v160
	s_waitcnt lgkmcnt(4)
	v_mfma_f32_32x32x16_bf16 v[64:79], v[226:229], v[136:139], v[64:79]
	v_add_f32_e32 v160, v108, v160
	v_add_f32_e32 v160, v109, v160
	v_add_f32_e32 v160, v110, v160
	v_add_f32_e32 v160, v111, v160
	s_waitcnt lgkmcnt(3)
	v_mfma_f32_32x32x16_bf16 v[80:95], v[230:233], v[132:135], v[80:95]
	v_mov_b32_e32 v161, v160
	s_nop 1
	v_permlane32_swap_b32_e32 v160, v161
	v_add_f32_e32 v160, v160, v161
	s_waitcnt lgkmcnt(2)
	v_mfma_f32_32x32x16_bf16 v[64:79], v[234:237], v[132:135], v[64:79]
	ds_read_b64_tr_b16 v[222:223], v181 offset:0
	ds_read_b64_tr_b16 v[224:225], v181 offset:2048
	ds_read_b64_tr_b16 v[226:227], v181 offset:4096
	ds_read_b64_tr_b16 v[228:229], v181 offset:6144
	ds_read_b64_tr_b16 v[230:231], v181 offset:8192
	ds_read_b64_tr_b16 v[232:233], v181 offset:10240
	ds_read_b64_tr_b16 v[234:235], v181 offset:12288
	ds_read_b64_tr_b16 v[236:237], v181 offset:14336
	v_add_f32_e32 v212, v212, v160
	v_cvt_pk_bf16_f32 v160, v112, v113
	v_cvt_pk_bf16_f32 v161, v114, v115
	v_cvt_pk_bf16_f32 v162, v116, v117
	s_waitcnt lgkmcnt(9)
	v_mfma_f32_32x32x16_bf16 v[80:95], v[238:241], v[128:131], v[80:95]
	v_cvt_pk_bf16_f32 v163, v118, v119
	v_cvt_pk_bf16_f32 v164, v120, v121
	v_cvt_pk_bf16_f32 v165, v122, v123
	v_cvt_pk_bf16_f32 v166, v124, v125
	s_waitcnt lgkmcnt(8)
	v_mfma_f32_32x32x16_bf16 v[64:79], v[242:245], v[128:131], v[64:79]
	v_cvt_pk_bf16_f32 v167, v126, v127
	v_cvt_pk_bf16_f32 v168, v96, v97
	v_cvt_pk_bf16_f32 v169, v98, v99
	v_cvt_pk_bf16_f32 v170, v100, v101
	ds_read_b64_tr_b16 v[246:247], v181 offset:512
	ds_read_b64_tr_b16 v[248:249], v181 offset:2560
	v_cvt_pk_bf16_f32 v171, v102, v103
	v_cvt_pk_bf16_f32 v172, v104, v105
	v_cvt_pk_bf16_f32 v173, v106, v107
	v_cvt_pk_bf16_f32 v174, v108, v109
	v_cvt_pk_bf16_f32 v175, v110, v111
	s_nop 0
	v_permlane32_swap_b32_e32 v160, v162
	v_permlane32_swap_b32_e32 v161, v163
	v_permlane32_swap_b32_e32 v164, v166
	v_permlane32_swap_b32_e32 v165, v167
	v_permlane32_swap_b32_e32 v168, v170
	v_permlane32_swap_b32_e32 v169, v171
	v_permlane32_swap_b32_e32 v172, v174
	v_permlane32_swap_b32_e32 v173, v175
	s_waitcnt lgkmcnt(8)
	v_mfma_f32_32x32x16_bf16 v[48:63], v[160:163], v[222:225], v[48:63]
	ds_read_b64_tr_b16 v[238:239], v181 offset:4608
	ds_read_b64_tr_b16 v[240:241], v181 offset:6656
	v_exp_f32_e32 v80, v80
	s_waitcnt lgkmcnt(8)
	v_mfma_f32_32x32x16_bf16 v[48:63], v[164:167], v[226:229], v[48:63]
	ds_read_b64_tr_b16 v[222:223], v181 offset:8704
	ds_read_b64_tr_b16 v[224:225], v181 offset:10752
	v_exp_f32_e32 v81, v81
	s_min_i32 s5, s65, s92
	s_lshl_b32 s72, s5, 16
	s_lshl_b32 s5, s87, 14
	s_addk_i32 s5, 0xc000
	s_cmp_gt_i32 s87, 0
	s_cselect_b32 s5, s5, 0x8000
	s_add_i32 s5, s64, s5
	s_add_i32 m0, s5, 0xc000
	s_add_u32 s56, s34, s72
	s_addc_u32 s57, s35, 0
	v_lshl_add_u64 v[250:251], v[186:187], 0, s[72:73]
	s_nop 0
	global_load_lds_dwordx4 v[250:251], off
	s_waitcnt lgkmcnt(8)
	v_mfma_f32_32x32x16_bf16 v[48:63], v[168:171], v[230:233], v[48:63]
	ds_read_b64_tr_b16 v[226:227], v181 offset:12800
	ds_read_b64_tr_b16 v[228:229], v181 offset:14848
	v_exp_f32_e32 v82, v82
	v_lshl_add_u64 v[250:251], v[176:177], 1, s[56:57]
	s_add_i32 m0, s5, 0xe000
	v_lshl_add_u64 v[250:251], v[250:251], 0, s[80:81]
	s_nop 0
	global_load_lds_dwordx4 v[250:251], off
	s_waitcnt lgkmcnt(8)
	v_mfma_f32_32x32x16_bf16 v[48:63], v[172:175], v[234:237], v[48:63]
	ds_read_b64_tr_b16 v[230:231], v181 offset:1024
	ds_read_b64_tr_b16 v[232:233], v181 offset:3072
	v_exp_f32_e32 v83, v83
	s_add_i32 s56, s86, 64
	s_ashr_i32 s57, s56, 31
	s_lshl_b64 s[56:57], s[56:57], 10
	s_lshl_b32 s20, s15, 14
	s_add_i32 s5, s20, 0xffffc000
	s_cmp_gt_i32 s15, 0
	s_cselect_b32 s5, s5, 0x8000
	s_add_i32 s5, s64, s5
	v_lshl_add_u64 v[250:251], v[188:189], 0, s[56:57]
	s_mov_b32 m0, s5
	s_nop 0
	global_load_lds_dwordx4 v[250:251], off
	s_waitcnt lgkmcnt(8)
	v_mfma_f32_32x32x16_bf16 v[32:47], v[160:163], v[246:249], v[32:47]
	ds_read_b64_tr_b16 v[234:235], v181 offset:5120
	ds_read_b64_tr_b16 v[236:237], v181 offset:7168
	v_exp_f32_e32 v84, v84
	s_add_i32 s56, s86, 0x60
	s_ashr_i32 s57, s56, 31
	s_lshl_b64 s[56:57], s[56:57], 10
	v_lshl_add_u64 v[250:251], v[188:189], 0, s[56:57]
	s_add_i32 m0, s5, 0x2000
	s_nop 0
	global_load_lds_dwordx4 v[250:251], off
	s_waitcnt lgkmcnt(8)
	v_mfma_f32_32x32x16_bf16 v[32:47], v[164:167], v[238:241], v[32:47]
	ds_read_b64_tr_b16 v[246:247], v181 offset:9216
	ds_read_b64_tr_b16 v[248:249], v181 offset:11264
	v_exp_f32_e32 v85, v85
	s_waitcnt lgkmcnt(8)
	v_mfma_f32_32x32x16_bf16 v[32:47], v[168:171], v[222:225], v[32:47]
	ds_read_b64_tr_b16 v[238:239], v181 offset:13312
	ds_read_b64_tr_b16 v[240:241], v181 offset:15360
	v_exp_f32_e32 v86, v86
	s_waitcnt lgkmcnt(8)
	v_mfma_f32_32x32x16_bf16 v[32:47], v[172:175], v[226:229], v[32:47]
	ds_read_b64_tr_b16 v[222:223], v181 offset:1536
	ds_read_b64_tr_b16 v[224:225], v181 offset:3584
	v_exp_f32_e32 v87, v87
	s_waitcnt lgkmcnt(8)
	v_mfma_f32_32x32x16_bf16 v[16:31], v[160:163], v[230:233], v[16:31]
	ds_read_b64_tr_b16 v[226:227], v181 offset:5632
	ds_read_b64_tr_b16 v[228:229], v181 offset:7680
	v_exp_f32_e32 v88, v88
	s_waitcnt lgkmcnt(8)
	v_mfma_f32_32x32x16_bf16 v[16:31], v[164:167], v[234:237], v[16:31]
	ds_read_b64_tr_b16 v[230:231], v181 offset:9728
	ds_read_b64_tr_b16 v[232:233], v181 offset:11776
	v_exp_f32_e32 v89, v89
	s_waitcnt lgkmcnt(8)
	v_mfma_f32_32x32x16_bf16 v[16:31], v[168:171], v[246:249], v[16:31]
	ds_read_b64_tr_b16 v[234:235], v181 offset:13824
	ds_read_b64_tr_b16 v[236:237], v181 offset:15872
	v_exp_f32_e32 v90, v90
	s_waitcnt lgkmcnt(8)
	v_mfma_f32_32x32x16_bf16 v[16:31], v[172:175], v[238:241], v[16:31]
	v_exp_f32_e32 v91, v91
	s_waitcnt lgkmcnt(6)
	v_mfma_f32_32x32x16_bf16 v[0:15], v[160:163], v[222:225], v[0:15]
	v_exp_f32_e32 v92, v92
	s_waitcnt lgkmcnt(4)
	v_mfma_f32_32x32x16_bf16 v[0:15], v[164:167], v[226:229], v[0:15]
	v_exp_f32_e32 v93, v93
	s_waitcnt lgkmcnt(2)
	v_mfma_f32_32x32x16_bf16 v[0:15], v[168:171], v[230:233], v[0:15]
	v_exp_f32_e32 v94, v94
	s_waitcnt lgkmcnt(0)
	v_mfma_f32_32x32x16_bf16 v[0:15], v[172:175], v[234:237], v[0:15]
	v_exp_f32_e32 v95, v95
	s_mov_b64 s[90:91], -1
	s_mov_b64 s[38:39], 0
	s_mov_b32 s89, s73
	s_add_i32 s5, s87, 1
	s_cmp_lt_i32 s87, 2
	s_cselect_b32 s89, s5, 0
	s_add_i32 s5, s15, 1
	s_waitcnt vmcnt(4) lgkmcnt(0)
	s_barrier
	s_cmp_lt_i32 s15, 2
	s_cselect_b32 s15, s5, 0
	s_add_i32 s88, s88, 4
	s_addk_i32 s86, 0x80
	v_lshl_add_u64 v[190:191], v[190:191], 0, s[16:17]
	s_cmp_ge_u32 s65, s18
	s_cbranch_scc1 .LBB0_1846
	s_add_i32 s20, s65, -1
	s_cmp_lt_i32 s20, s22
	s_cbranch_scc1 .Lfs_loop
	s_branch .LBB0_1830
